# baseline (speedup 1.0000x reference)
_Z5k_aggILi0EEvPKDF16_S1_S1_PK15HIP_vector_typeIiLj4EEPKiS7_PKfS1_S9_PfPDF16_S1_S9_SB_SB_:
	s_lshr_b32 s3, s2, 3
	s_and_b32 s3, s3, 0x18
	s_bcnt1_i32_b32 s3, s3
	s_bitcmp1_b32 s3, 0
	s_cbranch_scc0 .Lnosleep_a0_0
	s_sleep 127
	s_sleep 23

_Z5k_aggILi1EEvPKDF16_S1_S1_PK15HIP_vector_typeIiLj4EEPKiS7_PKfS1_S9_PfPDF16_S1_S9_SB_SB_:
	s_lshr_b32 s3, s2, 3
	s_and_b32 s3, s3, 0x18
	s_bcnt1_i32_b32 s3, s3
	s_bitcmp1_b32 s3, 0
	s_cbranch_scc0 .Lnosleep_a1_0
	s_sleep 127
	s_sleep 23
